# speedup vs baseline: 1.6304x; 1.6304x over previous
.LBB1_36:
	s_or_b64 exec, exec, s[2:3]
	s_waitcnt vmcnt(0)
	v_add_f32_e32 v103, 0, v103
	v_add_f32_e32 v103, v103, v104
	v_add_f32_e32 v103, v103, v105
	v_add_f32_e32 v103, v103, v106
	v_add_f32_e32 v103, v103, v107
	v_add_f32_e32 v103, v103, v108
	v_add_f32_e32 v103, v103, v109
	v_add_f32_e32 v103, v103, v110
	v_add_f32_e32 v103, v103, v111
	v_add_f32_e32 v103, v103, v112
	v_add_f32_e32 v103, v103, v113
	v_add_f32_e32 v103, v103, v114
	v_add_f32_e32 v103, v103, v115
	v_add_f32_e32 v103, v103, v116
	v_add_f32_e32 v103, v103, v117
	v_add_f32_e32 v103, v103, v118
	v_add_f32_e32 v103, v103, v119
	v_add_f32_e32 v103, v103, v120
	v_add_f32_e32 v103, v103, v121
	v_add_f32_e32 v103, v103, v122
	s_mov_b32 s14, 0xf800000
	s_mov_b32 s11, 0x41e6d4ca
	v_cmp_gt_f32_e32 vcc, s14, v103
	v_mul_f32_e32 v104, 0x4f800000, v103
	s_nop 0
	v_cndmask_b32_e32 v104, v103, v104, vcc
	v_sqrt_f32_e32 v103, v104
	s_nop 0
	v_add_u32_e32 v105, -1, v103
	v_fma_f32 v108, -v105, v103, v104
	v_cmp_ge_f32_e64 s[2:3], 0, v108
	v_add_u32_e32 v108, 1, v103
	s_nop 0
	v_cndmask_b32_e64 v105, v103, v105, s[2:3]
	v_fma_f32 v103, -v108, v103, v104
	v_cmp_lt_f32_e64 s[2:3], 0, v103
	s_nop 1
	v_cndmask_b32_e64 v103, v105, v108, s[2:3]
	v_mul_f32_e32 v105, 0x37800000, v103
	v_cndmask_b32_e32 v105, v103, v105, vcc
	v_mov_b32_e32 v103, 0x260
	v_cmp_class_f32_e32 vcc, v104, v103
	s_nop 1
	v_cndmask_b32_e32 v104, v105, v104, vcc
	v_add_f32_e32 v104, 0x322bcc77, v104
	v_div_scale_f32 v108, s[2:3], v104, v104, s11
	v_rcp_f32_e32 v105, v108
	s_nop 0
	v_fma_f32 v109, -v108, v105, 1.0
	v_fmac_f32_e32 v105, v109, v105
	v_div_scale_f32 v107, vcc, s11, v104, s11
	v_mul_f32_e32 v106, v107, v105
	v_fma_f32 v111, -v108, v106, v107
	v_fmac_f32_e32 v106, v111, v105
	v_fma_f32 v107, -v108, v106, v107
	s_nop 0
	v_div_fmas_f32 v109, v107, v105, v106
	v_div_fixup_f32 v109, v109, v104, s11
	v_lshlrev_b32_e32 v110, 2, v101
	ds_bpermute_b32 v64, v110, v109
	ds_bpermute_b32 v65, v110, v109 offset:64
	ds_bpermute_b32 v68, v110, v109 offset:128
	ds_bpermute_b32 v70, v110, v109 offset:192
	s_mul_i32 s2, s23, 0x1f80
	s_add_i32 s6, s8, s2
	s_movk_i32 s2, 0x88
	v_and_b32_e32 v66, 0x70, v100
	v_add_u32_e32 v71, s10, v66
	ds_read_b128 v[76:79], v71 offset:8832
	v_lshrrev_b32_e32 v67, 4, v100
	v_lshlrev_b32_e32 v67, 3, v67
	v_add_u32_e32 v72, s6, v67
	s_waitcnt lgkmcnt(0)
	v_mul_f32_e32 v73, v76, v64
	v_fmaak_f32 v60, v60, v73, 0xc1e6d4ca
	v_exp_f32_e32 v73, v60
	v_mul_f32_e32 v60, v77, v64
	v_fmaak_f32 v60, v61, v60, 0xc1e6d4ca
	v_mul_f32_e32 v61, v78, v64
	v_fmaak_f32 v61, v62, v61, 0xc1e6d4ca
	v_mul_f32_e32 v62, v79, v64
	v_fmaak_f32 v62, v63, v62, 0xc1e6d4ca
	v_exp_f32_e32 v61, v61
	v_exp_f32_e32 v62, v62
	v_exp_f32_e32 v74, v60
	v_mad_u32_u24 v60, v101, s2, v72
	s_mov_b32 s10, s9
	v_cvt_pk_bf16_f32 v63, v61, v62
	v_mul_f32_e32 v61, v76, v65
	v_fmaak_f32 v56, v56, v61, 0xc1e6d4ca
	v_mul_f32_e32 v61, v77, v65
	v_fmaak_f32 v57, v57, v61, 0xc1e6d4ca
	v_exp_f32_e32 v61, v57
	v_mul_f32_e32 v57, v78, v65
	v_cvt_pk_bf16_f32 v62, v73, v74
	v_fmaak_f32 v57, v58, v57, 0xc1e6d4ca
	ds_write_b64 v60, v[62:63] offset:10240
	v_exp_f32_e32 v62, v57
	v_mul_f32_e32 v57, v79, v65
	v_fmaak_f32 v57, v59, v57, 0xc1e6d4ca
	v_exp_f32_e32 v56, v56
	v_exp_f32_e32 v59, v57
	v_mov_b32_e32 v57, 0x880
	v_mad_u32_u24 v57, v101, s2, v57
	v_add_u32_e32 v58, v72, v57
	v_cvt_pk_bf16_f32 v63, v62, v59
	v_cvt_pk_bf16_f32 v62, v56, v61
	v_mul_f32_e32 v56, v76, v68
	v_fmaak_f32 v52, v52, v56, 0xc1e6d4ca
	v_exp_f32_e32 v56, v52
	v_mul_f32_e32 v52, v77, v68
	v_fmaak_f32 v52, v53, v52, 0xc1e6d4ca
	v_exp_f32_e32 v59, v52
	v_mul_f32_e32 v52, v78, v68
	v_fmaak_f32 v52, v54, v52, 0xc1e6d4ca
	v_exp_f32_e32 v54, v52
	v_mul_f32_e32 v52, v79, v68
	v_fmaak_f32 v52, v55, v52, 0xc1e6d4ca
	v_exp_f32_e32 v55, v52
	v_mov_b32_e32 v52, 0x1100
	v_mad_u32_u24 v52, v101, s2, v52
	v_add_u32_e32 v53, v72, v52
	v_cvt_pk_bf16_f32 v55, v54, v55
	v_cvt_pk_bf16_f32 v54, v56, v59
	ds_write_b64 v53, v[54:55] offset:10240
	v_mul_f32_e32 v54, v76, v70
	v_fmaak_f32 v48, v48, v54, 0xc1e6d4ca
	v_exp_f32_e32 v54, v48
	v_mul_f32_e32 v48, v77, v70
	v_fmaak_f32 v48, v49, v48, 0xc1e6d4ca
	v_exp_f32_e32 v49, v48
	v_mul_f32_e32 v48, v78, v70
	v_fmaak_f32 v48, v50, v48, 0xc1e6d4ca
	v_exp_f32_e32 v50, v48
	v_mul_f32_e32 v48, v79, v70
	v_fmaak_f32 v48, v51, v48, 0xc1e6d4ca
	v_exp_f32_e32 v51, v48
	v_mov_b32_e32 v48, 0x1980
	v_mad_u32_u24 v56, v101, s2, v48
	v_add_u32_e32 v48, v72, v56
	v_cvt_pk_bf16_f32 v51, v50, v51
	v_cvt_pk_bf16_f32 v50, v54, v49
	ds_write_b64 v58, v[62:63] offset:10240
	ds_write_b64 v48, v[50:51] offset:10240
	ds_read_b128 v[76:79], v71 offset:8896
	s_mov_b32 s11, s9
	s_waitcnt lgkmcnt(0)
	v_mul_f32_e32 v49, v76, v64
	v_fmaak_f32 v44, v44, v49, 0xc1e6d4ca
	v_mul_f32_e32 v49, v78, v64
	v_fmaak_f32 v46, v46, v49, 0xc1e6d4ca
	v_mul_f32_e32 v49, v79, v64
	v_fmaak_f32 v47, v47, v49, 0xc1e6d4ca
	v_exp_f32_e32 v46, v46
	v_exp_f32_e32 v47, v47
	v_mul_f32_e32 v49, v77, v64
	v_fmaak_f32 v45, v45, v49, 0xc1e6d4ca
	v_exp_f32_e32 v49, v45
	v_cvt_pk_bf16_f32 v45, v46, v47
	v_mul_f32_e32 v46, v76, v65
	v_fmaak_f32 v40, v40, v46, 0xc1e6d4ca
	v_mul_f32_e32 v46, v77, v65
	v_fmaak_f32 v41, v41, v46, 0xc1e6d4ca
	v_mul_f32_e32 v46, v78, v65
	v_fmaak_f32 v42, v42, v46, 0xc1e6d4ca
	v_mul_f32_e32 v46, v79, v65
	v_fmaak_f32 v43, v43, v46, 0xc1e6d4ca
	v_exp_f32_e32 v40, v40
	v_exp_f32_e32 v42, v42
	v_exp_f32_e32 v43, v43
	v_exp_f32_e32 v46, v41
	v_exp_f32_e32 v44, v44
	v_cvt_pk_bf16_f32 v41, v42, v43
	v_cvt_pk_bf16_f32 v40, v40, v46
	ds_write_b64 v58, v[40:41] offset:10272
	v_mul_f32_e32 v40, v76, v68
	v_fmaak_f32 v36, v36, v40, 0xc1e6d4ca
	v_mul_f32_e32 v40, v78, v68
	v_fmaak_f32 v38, v38, v40, 0xc1e6d4ca
	v_mul_f32_e32 v40, v79, v68
	v_fmaak_f32 v39, v39, v40, 0xc1e6d4ca
	v_exp_f32_e32 v38, v38
	v_exp_f32_e32 v39, v39
	v_mul_f32_e32 v40, v77, v68
	v_fmaak_f32 v37, v37, v40, 0xc1e6d4ca
	v_exp_f32_e32 v40, v37
	v_cvt_pk_bf16_f32 v37, v38, v39
	v_mul_f32_e32 v38, v76, v70
	v_fmaak_f32 v32, v32, v38, 0xc1e6d4ca
	v_mul_f32_e32 v38, v77, v70
	v_fmaak_f32 v33, v33, v38, 0xc1e6d4ca
	v_mul_f32_e32 v38, v78, v70
	v_fmaak_f32 v34, v34, v38, 0xc1e6d4ca
	v_mul_f32_e32 v38, v79, v70
	v_fmaak_f32 v35, v35, v38, 0xc1e6d4ca
	v_exp_f32_e32 v36, v36
	v_exp_f32_e32 v32, v32
	v_exp_f32_e32 v34, v34
	v_exp_f32_e32 v35, v35
	v_exp_f32_e32 v38, v33
	v_cvt_pk_bf16_f32 v44, v44, v49
	v_cvt_pk_bf16_f32 v36, v36, v40
	v_cvt_pk_bf16_f32 v33, v34, v35
	v_cvt_pk_bf16_f32 v32, v32, v38
	ds_write_b64 v60, v[44:45] offset:10272
	ds_write_b64 v53, v[36:37] offset:10272
	ds_write_b64 v48, v[32:33] offset:10272
	ds_read_b128 v[32:35], v71 offset:8960
	s_waitcnt lgkmcnt(0)
	v_mul_f32_e32 v36, v32, v64
	v_fmaak_f32 v28, v28, v36, 0xc1e6d4ca
	v_mul_f32_e32 v36, v34, v64
	v_fmaak_f32 v30, v30, v36, 0xc1e6d4ca
	v_mul_f32_e32 v36, v35, v64
	v_fmaak_f32 v31, v31, v36, 0xc1e6d4ca
	v_exp_f32_e32 v30, v30
	v_exp_f32_e32 v31, v31
	v_mul_f32_e32 v36, v33, v64
	v_fmaak_f32 v29, v29, v36, 0xc1e6d4ca
	v_exp_f32_e32 v36, v29
	v_cvt_pk_bf16_f32 v29, v30, v31
	v_mul_f32_e32 v30, v32, v65
	v_fmaak_f32 v24, v24, v30, 0xc1e6d4ca
	v_mul_f32_e32 v30, v33, v65
	v_fmaak_f32 v25, v25, v30, 0xc1e6d4ca
	v_mul_f32_e32 v30, v34, v65
	v_fmaak_f32 v26, v26, v30, 0xc1e6d4ca
	v_mul_f32_e32 v30, v35, v65
	v_fmaak_f32 v27, v27, v30, 0xc1e6d4ca
	v_exp_f32_e32 v24, v24
	v_exp_f32_e32 v26, v26
	v_exp_f32_e32 v27, v27
	v_exp_f32_e32 v30, v25
	v_exp_f32_e32 v28, v28
	v_cvt_pk_bf16_f32 v25, v26, v27
	v_cvt_pk_bf16_f32 v24, v24, v30
	ds_write_b64 v58, v[24:25] offset:10304
	v_mul_f32_e32 v24, v32, v68
	v_fmaak_f32 v20, v20, v24, 0xc1e6d4ca
	v_mul_f32_e32 v24, v34, v68
	v_fmaak_f32 v22, v22, v24, 0xc1e6d4ca
	v_mul_f32_e32 v24, v35, v68
	v_fmaak_f32 v23, v23, v24, 0xc1e6d4ca
	v_exp_f32_e32 v22, v22
	v_exp_f32_e32 v23, v23
	v_mul_f32_e32 v24, v33, v68
	v_fmaak_f32 v21, v21, v24, 0xc1e6d4ca
	v_exp_f32_e32 v24, v21
	v_cvt_pk_bf16_f32 v21, v22, v23
	v_mul_f32_e32 v22, v32, v70
	v_fmaak_f32 v16, v16, v22, 0xc1e6d4ca
	v_mul_f32_e32 v22, v33, v70
	v_fmaak_f32 v17, v17, v22, 0xc1e6d4ca
	v_mul_f32_e32 v22, v34, v70
	v_fmaak_f32 v18, v18, v22, 0xc1e6d4ca
	v_mul_f32_e32 v22, v35, v70
	v_fmaak_f32 v19, v19, v22, 0xc1e6d4ca
	v_exp_f32_e32 v20, v20
	v_exp_f32_e32 v16, v16
	v_exp_f32_e32 v18, v18
	v_exp_f32_e32 v19, v19
	v_exp_f32_e32 v22, v17
	v_cvt_pk_bf16_f32 v28, v28, v36
	v_cvt_pk_bf16_f32 v20, v20, v24
	v_cvt_pk_bf16_f32 v17, v18, v19
	v_cvt_pk_bf16_f32 v16, v16, v22
	ds_write_b64 v60, v[28:29] offset:10304
	ds_write_b64 v53, v[20:21] offset:10304
	ds_write_b64 v48, v[16:17] offset:10304
	ds_read_b128 v[16:19], v71 offset:9024
	v_mov_b32_e32 v20, 0xc1e6d4ca
	s_waitcnt lgkmcnt(0)
	v_mul_f32_e32 v21, v16, v64
	v_fmaak_f32 v12, v12, v21, 0xc1e6d4ca
	v_mul_f32_e32 v21, v18, v64
	v_fmaak_f32 v14, v14, v21, 0xc1e6d4ca
	v_mul_f32_e32 v21, v19, v64
	v_fmaak_f32 v15, v15, v21, 0xc1e6d4ca
	v_exp_f32_e32 v14, v14
	v_exp_f32_e32 v15, v15
	v_mul_f32_e32 v21, v17, v64
	v_fmaak_f32 v13, v13, v21, 0xc1e6d4ca
	v_exp_f32_e32 v21, v13
	v_cvt_pk_bf16_f32 v13, v14, v15
	v_mul_f32_e32 v14, v16, v65
	v_fmaak_f32 v8, v8, v14, 0xc1e6d4ca
	v_mul_f32_e32 v14, v17, v65
	v_fmaak_f32 v9, v9, v14, 0xc1e6d4ca
	v_mul_f32_e32 v14, v18, v65
	v_fmaak_f32 v10, v10, v14, 0xc1e6d4ca
	v_mul_f32_e32 v14, v19, v65
	v_fmaak_f32 v11, v11, v14, 0xc1e6d4ca
	v_exp_f32_e32 v8, v8
	v_exp_f32_e32 v10, v10
	v_exp_f32_e32 v11, v11
	v_exp_f32_e32 v14, v9
	v_exp_f32_e32 v12, v12
	v_and_b32_e32 v64, 1, v100
	v_cvt_pk_bf16_f32 v9, v10, v11
	v_cvt_pk_bf16_f32 v8, v8, v14
	ds_write_b64 v58, v[8:9] offset:10336
	v_mul_f32_e32 v8, v16, v68
	v_fmaak_f32 v4, v4, v8, 0xc1e6d4ca
	v_mul_f32_e32 v8, v18, v68
	v_fmaak_f32 v6, v6, v8, 0xc1e6d4ca
	v_mul_f32_e32 v8, v19, v68
	v_fmaak_f32 v7, v7, v8, 0xc1e6d4ca
	v_exp_f32_e32 v6, v6
	v_exp_f32_e32 v7, v7
	v_mul_f32_e32 v8, v17, v68
	v_fmaak_f32 v5, v5, v8, 0xc1e6d4ca
	v_exp_f32_e32 v8, v5
	v_cvt_pk_bf16_f32 v5, v6, v7
	v_mul_f32_e32 v6, v16, v70
	v_fmaak_f32 v0, v0, v6, 0xc1e6d4ca
	v_mul_f32_e32 v6, v17, v70
	v_fmaak_f32 v1, v1, v6, 0xc1e6d4ca
	v_mul_f32_e32 v6, v18, v70
	v_fmaak_f32 v2, v2, v6, 0xc1e6d4ca
	v_mul_f32_e32 v6, v19, v70
	v_fmac_f32_e32 v20, v3, v6
	v_exp_f32_e32 v0, v0
	v_exp_f32_e32 v2, v2
	v_exp_f32_e32 v3, v20
	v_exp_f32_e32 v6, v1
	v_exp_f32_e32 v4, v4
	v_cvt_pk_bf16_f32 v12, v12, v21
	v_cvt_pk_bf16_f32 v1, v2, v3
	v_cvt_pk_bf16_f32 v0, v0, v6
	ds_write_b64 v48, v[0:1] offset:10336
	v_lshrrev_b32_e32 v0, 2, v101
	v_or_b32_e32 v0, v67, v0
	v_lshlrev_b32_e32 v1, 3, v100
	v_mul_u32_u24_e32 v0, 0x88, v0
	v_and_b32_e32 v1, 24, v1
	v_add_u32_e32 v2, s6, v66
	v_cvt_pk_bf16_f32 v4, v4, v8
	v_add3_u32 v62, s6, v0, v1
	v_mad_u32_u24 v0, v101, s2, v2
	ds_write_b64 v60, v[12:13] offset:10336
	ds_write_b64 v53, v[4:5] offset:10336
	s_movk_i32 s34, 0x88
	v_and_b32_e32 v64, 32, v100
	v_and_b32_e32 v66, 16, v100
	v_mad_u32_u24 v65, v101, s34, v64
	v_add_u32_e32 v65, s6, v65
	v_add_u32_e32 v67, v65, v66
	v_sub_u32_e32 v65, v65, v66
	v_lshrrev_b32_e32 v68, 1, v100
	v_and_b32_e32 v68, 16, v68
	v_bfe_u32 v69, v100, 2, 2
	v_or_b32_e32 v68, v68, v69
	v_and_b32_e32 v69, 3, v100
	v_lshlrev_b32_e32 v69, 3, v69
	v_mad_u32_u24 v68, v68, s34, v69
	v_add_u32_e32 v68, s6, v68
	s_movk_i32 s35, 0x44
	v_mul_u32_u24_e32 v66, s35, v66
	v_add_u32_e32 v69, v68, v66
	v_sub_u32_e32 v68, v68, v66
	ds_read_b64 v[0:1], v67 offset:10240
	ds_read_b64 v[2:3], v65 offset:10264
	ds_read_b64 v[4:5], v67 offset:10304
	ds_read_b64 v[6:7], v65 offset:10328
	ds_read_b64 v[8:9], v67 offset:12424
	ds_read_b64 v[10:11], v67 offset:12416
	ds_read_b64 v[12:13], v67 offset:12488
	ds_read_b64 v[14:15], v67 offset:12480
	ds_read_b64 v[16:17], v65 offset:14608
	ds_read_b64 v[18:19], v67 offset:14600
	ds_read_b64 v[20:21], v65 offset:14672
	ds_read_b64 v[22:23], v67 offset:14664
	ds_read_b64 v[24:25], v65 offset:16792
	ds_read_b64 v[26:27], v65 offset:16784
	ds_read_b64 v[28:29], v65 offset:16856
	ds_read_b64 v[30:31], v65 offset:16848
	ds_read_b64_tr_b16 v[32:33], v69 offset:10240
	ds_read_b64_tr_b16 v[34:35], v68 offset:11872
	ds_read_b64_tr_b16 v[36:37], v69 offset:14592
	ds_read_b64_tr_b16 v[38:39], v68 offset:16224
	ds_read_b64_tr_b16 v[40:41], v69 offset:10816
	ds_read_b64_tr_b16 v[42:43], v69 offset:10272
	ds_read_b64_tr_b16 v[44:45], v69 offset:15168
	ds_read_b64_tr_b16 v[46:47], v69 offset:14624
	ds_read_b64_tr_b16 v[48:49], v68 offset:11392
	ds_read_b64_tr_b16 v[50:51], v69 offset:10848
	ds_read_b64_tr_b16 v[52:53], v68 offset:15744
	ds_read_b64_tr_b16 v[54:55], v69 offset:15200
	ds_read_b64_tr_b16 v[56:57], v68 offset:11968
	ds_read_b64_tr_b16 v[58:59], v68 offset:11424
	ds_read_b64_tr_b16 v[60:61], v68 offset:16320
	ds_read_b64_tr_b16 v[62:63], v68 offset:15776
	ds_read2st64_b32 v[116:117], v102 offset0:22 offset1:23
	v_and_b32_e32 v110, 1, v100
	v_cmp_eq_u32_e32 vcc, 0, v110
	v_mov_b32_e32 v110, 0xeeeeeeee
	v_mov_b32_e32 v111, 0x44444444
	s_mov_b32 s32, 0x2b8cbccc
	s_mov_b32 s33, 0
	v_cndmask_b32_e32 v64, v110, v111, vcc
	v_mov_b32_e32 v68, 0x3f803f80
	v_mov_b32_e32 v69, v68
	v_mov_b32_e32 v70, v68
	v_mov_b32_e32 v71, v68
	v_mov_b64_e32 v[72:73], s[32:33]
	v_mov_b64_e32 v[76:77], s[32:33]
	v_mov_b64_e32 v[80:81], s[32:33]
	v_mov_b64_e32 v[84:85], s[32:33]
	v_mov_b64_e32 v[88:89], s[32:33]
	v_mov_b64_e32 v[92:93], s[32:33]
	v_mov_b64_e32 v[96:97], s[32:33]
	v_mov_b64_e32 v[104:105], s[32:33]
	s_movk_i32 s30, 100
	v_mov_b32_e32 v122, 0
	s_waitcnt lgkmcnt(0)
	v_mov_b32_dpp v112, v116 quad_perm:[0,2,0,2] row_mask:0xf bank_mask:0xf
	v_mov_b32_dpp v113, v116 quad_perm:[1,3,1,3] row_mask:0xf bank_mask:0xf
	v_mov_b32_dpp v114, v117 quad_perm:[0,2,0,2] row_mask:0xf bank_mask:0xf
	v_mov_b32_dpp v115, v117 quad_perm:[1,3,1,3] row_mask:0xf bank_mask:0xf
	v_smfmac_f32_16x16x64_bf16 v[72:75], v[68:71], v[0:7], v64
	v_smfmac_f32_16x16x64_bf16 v[76:79], v[68:71], v[8:15], v64
	v_smfmac_f32_16x16x64_bf16 v[80:83], v[68:71], v[16:23], v64
	v_smfmac_f32_16x16x64_bf16 v[84:87], v[68:71], v[24:31], v64
	s_nop 0
.Lsk_loop:
	s_nop 3
	v_add_f32_dpp v108, v72, v73 quad_perm:[0,1,2,3] row_mask:0x1 bank_mask:0xf
	v_add_f32_dpp v108, v76, v77 quad_perm:[0,1,2,3] row_mask:0x2 bank_mask:0xf
	v_add_f32_dpp v108, v80, v81 quad_perm:[0,1,2,3] row_mask:0x4 bank_mask:0xf
	v_add_f32_dpp v108, v84, v85 quad_perm:[0,1,2,3] row_mask:0x8 bank_mask:0xf
	v_rcp_f32_e32 v109, v108
	v_mov_b64_e32 v[88:89], s[32:33]
	v_mov_b64_e32 v[92:93], s[32:33]
	v_mul_f32_dpp v110, v109, v114 quad_perm:[0,2,0,2] row_mask:0xf bank_mask:0xf
	v_mul_f32_dpp v111, v109, v115 quad_perm:[1,3,1,3] row_mask:0xf bank_mask:0xf
	v_cvt_pk_bf16_f32 v68, v110, v111
	v_mov_b64_e32 v[96:97], s[32:33]
	v_mov_b64_e32 v[104:105], s[32:33]
	v_mov_b32_dpp v69, v68 row_ror:4 row_mask:0xf bank_mask:0xf
	v_mov_b32_dpp v70, v68 row_ror:8 row_mask:0xf bank_mask:0xf
	v_mov_b32_dpp v71, v68 row_ror:12 row_mask:0xf bank_mask:0xf
	s_nop 1
	v_smfmac_f32_16x16x64_bf16 v[88:91], v[68:71], v[32:39], v64
	v_smfmac_f32_16x16x64_bf16 v[92:95], v[68:71], v[40:47], v64
	v_smfmac_f32_16x16x64_bf16 v[96:99], v[68:71], v[48:55], v64
	v_smfmac_f32_16x16x64_bf16 v[104:107], v[68:71], v[56:63], v64
	s_nop 4
	v_add_f32_dpp v108, v88, v89 quad_perm:[0,1,2,3] row_mask:0x1 bank_mask:0xf
	v_add_f32_dpp v108, v92, v93 quad_perm:[0,1,2,3] row_mask:0x2 bank_mask:0xf
	v_add_f32_dpp v108, v96, v97 quad_perm:[0,1,2,3] row_mask:0x4 bank_mask:0xf
	v_add_f32_dpp v108, v104, v105 quad_perm:[0,1,2,3] row_mask:0x8 bank_mask:0xf
	v_rcp_f32_e32 v109, v108
	v_mov_b64_e32 v[72:73], s[32:33]
	v_mov_b64_e32 v[76:77], s[32:33]
	v_mul_f32_dpp v110, v109, v112 quad_perm:[0,2,0,2] row_mask:0xf bank_mask:0xf
	v_mul_f32_dpp v111, v109, v113 quad_perm:[1,3,1,3] row_mask:0xf bank_mask:0xf
	v_cvt_pk_bf16_f32 v68, v110, v111
	v_mov_b64_e32 v[80:81], s[32:33]
	v_mov_b64_e32 v[84:85], s[32:33]
	v_mov_b32_dpp v69, v68 row_ror:4 row_mask:0xf bank_mask:0xf
	v_mov_b32_dpp v70, v68 row_ror:8 row_mask:0xf bank_mask:0xf
	v_mov_b32_dpp v71, v68 row_ror:12 row_mask:0xf bank_mask:0xf
	v_cmp_ne_u32_e32 vcc, v68, v122
	v_mov_b32_e32 v122, v68
	s_cmp_eq_u64 vcc, 0
	s_cselect_b32 s30, 1, s30
	s_add_i32 s30, s30, -1
	s_cmp_lg_u32 s30, 0
	v_smfmac_f32_16x16x64_bf16 v[72:75], v[68:71], v[0:7], v64
	v_smfmac_f32_16x16x64_bf16 v[76:79], v[68:71], v[8:15], v64
	v_smfmac_f32_16x16x64_bf16 v[80:83], v[68:71], v[16:23], v64
	v_smfmac_f32_16x16x64_bf16 v[84:87], v[68:71], v[24:31], v64
	s_cbranch_scc1 .Lsk_loop
	s_nop 3
	v_add_f32_dpp v108, v72, v73 quad_perm:[0,1,2,3] row_mask:0x1 bank_mask:0xf
	v_add_f32_dpp v108, v76, v77 quad_perm:[0,1,2,3] row_mask:0x2 bank_mask:0xf
	v_add_f32_dpp v108, v80, v81 quad_perm:[0,1,2,3] row_mask:0x4 bank_mask:0xf
	v_add_f32_dpp v108, v84, v85 quad_perm:[0,1,2,3] row_mask:0x8 bank_mask:0xf
	v_rcp_f32_e32 v109, v108
	s_mov_b32 s34, 0x3d0df4e0
	s_mov_b32 s35, s34
	v_mul_f32_e32 v118, v117, v109
	v_lshlrev_b32_e32 v72, 16, v0
	v_and_b32_e32 v73, 0xffff0000, v0
	v_log_f32_e32 v74, v72
	v_log_f32_e32 v75, v73
	s_nop 0
	v_pk_fma_f32 v[74:75], v[74:75], s[34:35], 1.0 op_sel_hi:[1,0,0]
	v_pk_mul_f32 v[74:75], v[74:75], v[72:73]
	v_cvt_pk_bf16_f32 v0, v74, v75
	v_lshlrev_b32_e32 v76, 16, v1
	v_and_b32_e32 v77, 0xffff0000, v1
	v_log_f32_e32 v78, v76
	v_log_f32_e32 v79, v77
	s_nop 0
	v_pk_fma_f32 v[78:79], v[78:79], s[34:35], 1.0 op_sel_hi:[1,0,0]
	v_pk_mul_f32 v[78:79], v[78:79], v[76:77]
	v_cvt_pk_bf16_f32 v1, v78, v79
	v_lshlrev_b32_e32 v80, 16, v2
	v_and_b32_e32 v81, 0xffff0000, v2
	v_log_f32_e32 v82, v80
	v_log_f32_e32 v83, v81
	s_nop 0
	v_pk_fma_f32 v[82:83], v[82:83], s[34:35], 1.0 op_sel_hi:[1,0,0]
	v_pk_mul_f32 v[82:83], v[82:83], v[80:81]
	v_cvt_pk_bf16_f32 v2, v82, v83
	v_lshlrev_b32_e32 v84, 16, v3
	v_and_b32_e32 v85, 0xffff0000, v3
	v_log_f32_e32 v86, v84
	v_log_f32_e32 v87, v85
	s_nop 0
	v_pk_fma_f32 v[86:87], v[86:87], s[34:35], 1.0 op_sel_hi:[1,0,0]
	v_pk_mul_f32 v[86:87], v[86:87], v[84:85]
	v_cvt_pk_bf16_f32 v3, v86, v87
	v_lshlrev_b32_e32 v72, 16, v4
	v_and_b32_e32 v73, 0xffff0000, v4
	v_log_f32_e32 v74, v72
	v_log_f32_e32 v75, v73
	s_nop 0
	v_pk_fma_f32 v[74:75], v[74:75], s[34:35], 1.0 op_sel_hi:[1,0,0]
	v_pk_mul_f32 v[74:75], v[74:75], v[72:73]
	v_cvt_pk_bf16_f32 v4, v74, v75
	v_lshlrev_b32_e32 v76, 16, v5
	v_and_b32_e32 v77, 0xffff0000, v5
	v_log_f32_e32 v78, v76
	v_log_f32_e32 v79, v77
	s_nop 0
	v_pk_fma_f32 v[78:79], v[78:79], s[34:35], 1.0 op_sel_hi:[1,0,0]
	v_pk_mul_f32 v[78:79], v[78:79], v[76:77]
	v_cvt_pk_bf16_f32 v5, v78, v79
	v_lshlrev_b32_e32 v80, 16, v6
	v_and_b32_e32 v81, 0xffff0000, v6
	v_log_f32_e32 v82, v80
	v_log_f32_e32 v83, v81
	s_nop 0
	v_pk_fma_f32 v[82:83], v[82:83], s[34:35], 1.0 op_sel_hi:[1,0,0]
	v_pk_mul_f32 v[82:83], v[82:83], v[80:81]
	v_cvt_pk_bf16_f32 v6, v82, v83
	v_lshlrev_b32_e32 v84, 16, v7
	v_and_b32_e32 v85, 0xffff0000, v7
	v_log_f32_e32 v86, v84
	v_log_f32_e32 v87, v85
	s_nop 0
	v_pk_fma_f32 v[86:87], v[86:87], s[34:35], 1.0 op_sel_hi:[1,0,0]
	v_pk_mul_f32 v[86:87], v[86:87], v[84:85]
	v_cvt_pk_bf16_f32 v7, v86, v87
	v_lshlrev_b32_e32 v72, 16, v8
	v_and_b32_e32 v73, 0xffff0000, v8
	v_log_f32_e32 v74, v72
	v_log_f32_e32 v75, v73
	s_nop 0
	v_pk_fma_f32 v[74:75], v[74:75], s[34:35], 1.0 op_sel_hi:[1,0,0]
	v_pk_mul_f32 v[74:75], v[74:75], v[72:73]
	v_cvt_pk_bf16_f32 v8, v74, v75
	v_lshlrev_b32_e32 v76, 16, v9
	v_and_b32_e32 v77, 0xffff0000, v9
	v_log_f32_e32 v78, v76
	v_log_f32_e32 v79, v77
	s_nop 0
	v_pk_fma_f32 v[78:79], v[78:79], s[34:35], 1.0 op_sel_hi:[1,0,0]
	v_pk_mul_f32 v[78:79], v[78:79], v[76:77]
	v_cvt_pk_bf16_f32 v9, v78, v79
	v_lshlrev_b32_e32 v80, 16, v10
	v_and_b32_e32 v81, 0xffff0000, v10
	v_log_f32_e32 v82, v80
	v_log_f32_e32 v83, v81
	s_nop 0
	v_pk_fma_f32 v[82:83], v[82:83], s[34:35], 1.0 op_sel_hi:[1,0,0]
	v_pk_mul_f32 v[82:83], v[82:83], v[80:81]
	v_cvt_pk_bf16_f32 v10, v82, v83
	v_lshlrev_b32_e32 v84, 16, v11
	v_and_b32_e32 v85, 0xffff0000, v11
	v_log_f32_e32 v86, v84
	v_log_f32_e32 v87, v85
	s_nop 0
	v_pk_fma_f32 v[86:87], v[86:87], s[34:35], 1.0 op_sel_hi:[1,0,0]
	v_pk_mul_f32 v[86:87], v[86:87], v[84:85]
	v_cvt_pk_bf16_f32 v11, v86, v87
	v_lshlrev_b32_e32 v72, 16, v12
	v_and_b32_e32 v73, 0xffff0000, v12
	v_log_f32_e32 v74, v72
	v_log_f32_e32 v75, v73
	s_nop 0
	v_pk_fma_f32 v[74:75], v[74:75], s[34:35], 1.0 op_sel_hi:[1,0,0]
	v_pk_mul_f32 v[74:75], v[74:75], v[72:73]
	v_cvt_pk_bf16_f32 v12, v74, v75
	v_lshlrev_b32_e32 v76, 16, v13
	v_and_b32_e32 v77, 0xffff0000, v13
	v_log_f32_e32 v78, v76
	v_log_f32_e32 v79, v77
	s_nop 0
	v_pk_fma_f32 v[78:79], v[78:79], s[34:35], 1.0 op_sel_hi:[1,0,0]
	v_pk_mul_f32 v[78:79], v[78:79], v[76:77]
	v_cvt_pk_bf16_f32 v13, v78, v79
	v_lshlrev_b32_e32 v80, 16, v14
	v_and_b32_e32 v81, 0xffff0000, v14
	v_log_f32_e32 v82, v80
	v_log_f32_e32 v83, v81
	s_nop 0
	v_pk_fma_f32 v[82:83], v[82:83], s[34:35], 1.0 op_sel_hi:[1,0,0]
	v_pk_mul_f32 v[82:83], v[82:83], v[80:81]
	v_cvt_pk_bf16_f32 v14, v82, v83
	v_lshlrev_b32_e32 v84, 16, v15
	v_and_b32_e32 v85, 0xffff0000, v15
	v_log_f32_e32 v86, v84
	v_log_f32_e32 v87, v85
	s_nop 0
	v_pk_fma_f32 v[86:87], v[86:87], s[34:35], 1.0 op_sel_hi:[1,0,0]
	v_pk_mul_f32 v[86:87], v[86:87], v[84:85]
	v_cvt_pk_bf16_f32 v15, v86, v87
	v_lshlrev_b32_e32 v72, 16, v16
	v_and_b32_e32 v73, 0xffff0000, v16
	v_log_f32_e32 v74, v72
	v_log_f32_e32 v75, v73
	s_nop 0
	v_pk_fma_f32 v[74:75], v[74:75], s[34:35], 1.0 op_sel_hi:[1,0,0]
	v_pk_mul_f32 v[74:75], v[74:75], v[72:73]
	v_cvt_pk_bf16_f32 v16, v74, v75
	v_lshlrev_b32_e32 v76, 16, v17
	v_and_b32_e32 v77, 0xffff0000, v17
	v_log_f32_e32 v78, v76
	v_log_f32_e32 v79, v77
	s_nop 0
	v_pk_fma_f32 v[78:79], v[78:79], s[34:35], 1.0 op_sel_hi:[1,0,0]
	v_pk_mul_f32 v[78:79], v[78:79], v[76:77]
	v_cvt_pk_bf16_f32 v17, v78, v79
	v_lshlrev_b32_e32 v80, 16, v18
	v_and_b32_e32 v81, 0xffff0000, v18
	v_log_f32_e32 v82, v80
	v_log_f32_e32 v83, v81
	s_nop 0
	v_pk_fma_f32 v[82:83], v[82:83], s[34:35], 1.0 op_sel_hi:[1,0,0]
	v_pk_mul_f32 v[82:83], v[82:83], v[80:81]
	v_cvt_pk_bf16_f32 v18, v82, v83
	v_lshlrev_b32_e32 v84, 16, v19
	v_and_b32_e32 v85, 0xffff0000, v19
	v_log_f32_e32 v86, v84
	v_log_f32_e32 v87, v85
	s_nop 0
	v_pk_fma_f32 v[86:87], v[86:87], s[34:35], 1.0 op_sel_hi:[1,0,0]
	v_pk_mul_f32 v[86:87], v[86:87], v[84:85]
	v_cvt_pk_bf16_f32 v19, v86, v87
	v_lshlrev_b32_e32 v72, 16, v20
	v_and_b32_e32 v73, 0xffff0000, v20
	v_log_f32_e32 v74, v72
	v_log_f32_e32 v75, v73
	s_nop 0
	v_pk_fma_f32 v[74:75], v[74:75], s[34:35], 1.0 op_sel_hi:[1,0,0]
	v_pk_mul_f32 v[74:75], v[74:75], v[72:73]
	v_cvt_pk_bf16_f32 v20, v74, v75
	v_lshlrev_b32_e32 v76, 16, v21
	v_and_b32_e32 v77, 0xffff0000, v21
	v_log_f32_e32 v78, v76
	v_log_f32_e32 v79, v77
	s_nop 0
	v_pk_fma_f32 v[78:79], v[78:79], s[34:35], 1.0 op_sel_hi:[1,0,0]
	v_pk_mul_f32 v[78:79], v[78:79], v[76:77]
	v_cvt_pk_bf16_f32 v21, v78, v79
	v_lshlrev_b32_e32 v80, 16, v22
	v_and_b32_e32 v81, 0xffff0000, v22
	v_log_f32_e32 v82, v80
	v_log_f32_e32 v83, v81
	s_nop 0
	v_pk_fma_f32 v[82:83], v[82:83], s[34:35], 1.0 op_sel_hi:[1,0,0]
	v_pk_mul_f32 v[82:83], v[82:83], v[80:81]
	v_cvt_pk_bf16_f32 v22, v82, v83
	v_lshlrev_b32_e32 v84, 16, v23
	v_and_b32_e32 v85, 0xffff0000, v23
	v_log_f32_e32 v86, v84
	v_log_f32_e32 v87, v85
	s_nop 0
	v_pk_fma_f32 v[86:87], v[86:87], s[34:35], 1.0 op_sel_hi:[1,0,0]
	v_pk_mul_f32 v[86:87], v[86:87], v[84:85]
	v_cvt_pk_bf16_f32 v23, v86, v87
	v_lshlrev_b32_e32 v72, 16, v24
	v_and_b32_e32 v73, 0xffff0000, v24
	v_log_f32_e32 v74, v72
	v_log_f32_e32 v75, v73
	s_nop 0
	v_pk_fma_f32 v[74:75], v[74:75], s[34:35], 1.0 op_sel_hi:[1,0,0]
	v_pk_mul_f32 v[74:75], v[74:75], v[72:73]
	v_cvt_pk_bf16_f32 v24, v74, v75
	v_lshlrev_b32_e32 v76, 16, v25
	v_and_b32_e32 v77, 0xffff0000, v25
	v_log_f32_e32 v78, v76
	v_log_f32_e32 v79, v77
	s_nop 0
	v_pk_fma_f32 v[78:79], v[78:79], s[34:35], 1.0 op_sel_hi:[1,0,0]
	v_pk_mul_f32 v[78:79], v[78:79], v[76:77]
	v_cvt_pk_bf16_f32 v25, v78, v79
	v_lshlrev_b32_e32 v80, 16, v26
	v_and_b32_e32 v81, 0xffff0000, v26
	v_log_f32_e32 v82, v80
	v_log_f32_e32 v83, v81
	s_nop 0
	v_pk_fma_f32 v[82:83], v[82:83], s[34:35], 1.0 op_sel_hi:[1,0,0]
	v_pk_mul_f32 v[82:83], v[82:83], v[80:81]
	v_cvt_pk_bf16_f32 v26, v82, v83
	v_lshlrev_b32_e32 v84, 16, v27
	v_and_b32_e32 v85, 0xffff0000, v27
	v_log_f32_e32 v86, v84
	v_log_f32_e32 v87, v85
	s_nop 0
	v_pk_fma_f32 v[86:87], v[86:87], s[34:35], 1.0 op_sel_hi:[1,0,0]
	v_pk_mul_f32 v[86:87], v[86:87], v[84:85]
	v_cvt_pk_bf16_f32 v27, v86, v87
	v_lshlrev_b32_e32 v72, 16, v28
	v_and_b32_e32 v73, 0xffff0000, v28
	v_log_f32_e32 v74, v72
	v_log_f32_e32 v75, v73
	s_nop 0
	v_pk_fma_f32 v[74:75], v[74:75], s[34:35], 1.0 op_sel_hi:[1,0,0]
	v_pk_mul_f32 v[74:75], v[74:75], v[72:73]
	v_cvt_pk_bf16_f32 v28, v74, v75
	v_lshlrev_b32_e32 v76, 16, v29
	v_and_b32_e32 v77, 0xffff0000, v29
	v_log_f32_e32 v78, v76
	v_log_f32_e32 v79, v77
	s_nop 0
	v_pk_fma_f32 v[78:79], v[78:79], s[34:35], 1.0 op_sel_hi:[1,0,0]
	v_pk_mul_f32 v[78:79], v[78:79], v[76:77]
	v_cvt_pk_bf16_f32 v29, v78, v79
	v_lshlrev_b32_e32 v80, 16, v30
	v_and_b32_e32 v81, 0xffff0000, v30
	v_log_f32_e32 v82, v80
	v_log_f32_e32 v83, v81
	s_nop 0
	v_pk_fma_f32 v[82:83], v[82:83], s[34:35], 1.0 op_sel_hi:[1,0,0]
	v_pk_mul_f32 v[82:83], v[82:83], v[80:81]
	v_cvt_pk_bf16_f32 v30, v82, v83
	v_lshlrev_b32_e32 v84, 16, v31
	v_and_b32_e32 v85, 0xffff0000, v31
	v_log_f32_e32 v86, v84
	v_log_f32_e32 v87, v85
	s_nop 0
	v_pk_fma_f32 v[86:87], v[86:87], s[34:35], 1.0 op_sel_hi:[1,0,0]
	v_pk_mul_f32 v[86:87], v[86:87], v[84:85]
	v_cvt_pk_bf16_f32 v31, v86, v87
	v_mov_b64_e32 v[88:89], s[32:33]
	v_mov_b64_e32 v[92:93], s[32:33]
	v_mov_b64_e32 v[96:97], s[32:33]
	v_mov_b64_e32 v[104:105], s[32:33]
	s_nop 1
	v_smfmac_f32_16x16x64_bf16 v[88:91], v[68:71], v[0:7], v64
	v_smfmac_f32_16x16x64_bf16 v[92:95], v[68:71], v[8:15], v64
	v_smfmac_f32_16x16x64_bf16 v[96:99], v[68:71], v[16:23], v64
	v_smfmac_f32_16x16x64_bf16 v[104:107], v[68:71], v[24:31], v64
	s_nop 4
	v_add_f32_dpp v108, v88, v89 quad_perm:[0,1,2,3] row_mask:0x1 bank_mask:0xf
	v_add_f32_dpp v108, v92, v93 quad_perm:[0,1,2,3] row_mask:0x2 bank_mask:0xf
	v_add_f32_dpp v108, v96, v97 quad_perm:[0,1,2,3] row_mask:0x4 bank_mask:0xf
	v_add_f32_dpp v108, v104, v105 quad_perm:[0,1,2,3] row_mask:0x8 bank_mask:0xf
	v_add_f32_e32 v108, 0xab8cbccc, v108
	v_mul_f32_e32 v108, v118, v108
	s_nop 1
	v_add_f32_dpp v108, v108, v108 row_ror:8 row_mask:0xf bank_mask:0xf
	s_nop 1
	v_add_f32_dpp v108, v108, v108 row_ror:4 row_mask:0xf bank_mask:0xf
	s_nop 1
	v_add_f32_dpp v108, v108, v108 row_ror:2 row_mask:0xf bank_mask:0xf
	s_nop 1
	v_add_f32_dpp v108, v108, v108 row_ror:1 row_mask:0xf bank_mask:0xf
	s_nop 1
	v_mov_b32_e32 v109, v108
	s_nop 1
	v_permlane16_swap_b32_e32 v108, v109
	v_add_f32_e32 v108, v108, v109
	v_mov_b32_e32 v109, v108
	s_nop 1
	v_permlane32_swap_b32_e32 v108, v109
	v_add_f32_e32 v108, v108, v109
	v_cmp_eq_u32_e32 vcc, 0, v100
	s_and_saveexec_b64 s[0:1], vcc
	s_cbranch_execz .LBB1_38
	s_mul_i32 s0, s22, 5
	s_add_i32 s0, s0, s23
	s_mov_b32 s1, 0
	s_lshl_b64 s[0:1], s[0:1], 2
	s_add_u32 s0, s12, s0
	s_addc_u32 s1, s13, s1
	v_mov_b32_e32 v109, 0
	global_store_dword v109, v108, s[0:1]
